# P0 W1/W2 conversion: drop the per-chunk vmcnt ladder (it waited for the NEXT item's loads); wait once in the preheader and before the first copy of the next item's registers
# baseline (speedup 1.0000x reference)
.LBB0_111:
	s_mov_b32 s4, 20
	s_waitcnt vmcnt(2)
	v_mov_b32_e32 v10, v0
	s_nop 0
	v_readfirstlane_b32 s5, v10
	s_ashr_i32 s6, s5, 6
	s_add_i32 s8, s6, s3
	s_cmp_gt_i32 s8, 0xffff
	s_cbranch_scc1 .LBB0_116
	s_ashr_i32 s5, s4, 31
	s_lshl_b64 s[4:5], s[4:5], 3
	s_add_u32 s4, s94, s4
	s_addc_u32 s5, s95, s5
	s_lshl_b32 s6, s6, 14
	s_add_i32 s9, s6, 0
	s_ashr_i32 s6, s8, 31
	s_load_dwordx2 s[4:5], s[4:5], 0x0
	s_lshr_b32 s6, s6, 23
	s_add_i32 s10, s8, s6
	s_ashr_i32 s6, s10, 9
	s_ashr_i32 s7, s6, 31
	s_lshl_b64 s[6:7], s[6:7], 23
	s_waitcnt lgkmcnt(0)
	s_add_u32 s11, s4, s6
	s_addc_u32 s12, s5, s7
	s_and_b32 s6, s10, 0xfffffe00
	s_sub_i32 s6, s8, s6
	s_ashr_i32 s7, s6, 31
	s_lshr_b32 s7, s7, 26
	s_add_i32 s7, s6, s7
	s_and_b32 s10, s7, 0x7ffffc0
	s_sub_i32 s6, s6, s10
	s_lshl_b32 s7, s7, 1
	s_and_b32 s7, s7, 0xffffff80
	s_lshl_b32 s6, s6, 5
	v_bfe_u32 v1, v10, 3, 3
	s_waitcnt vmcnt(0)
	v_or_b32_e32 v2, s7, v1
	s_ashr_i32 s7, s6, 31
	s_lshl_b64 s[6:7], s[6:7], 2
	v_lshlrev_b32_e32 v3, 2, v10
	s_add_u32 s6, s11, s6
	v_and_b32_e32 v12, 28, v3
	s_addc_u32 s7, s12, s7
	v_mov_b32_e32 v137, 0
	v_lshlrev_b32_e32 v136, 2, v12
	v_ashrrev_i32_e32 v3, 31, v2
	v_or_b32_e32 v8, 8, v2
	v_lshl_add_u64 v[4:5], s[6:7], 0, v[136:137]
	v_lshlrev_b64 v[6:7], 13, v[2:3]
	v_ashrrev_i32_e32 v9, 31, v8
	v_lshl_add_u64 v[6:7], v[4:5], 0, v[6:7]
	v_lshlrev_b64 v[8:9], 13, v[8:9]
	v_lshl_add_u64 v[8:9], v[4:5], 0, v[8:9]
	global_load_dwordx4 v[126:129], v[6:7], off nt
	global_load_dwordx4 v[122:125], v[8:9], off nt
	v_or_b32_e32 v6, 16, v2
	v_ashrrev_i32_e32 v7, 31, v6
	v_or_b32_e32 v8, 24, v2
	v_lshlrev_b64 v[6:7], 13, v[6:7]
	v_ashrrev_i32_e32 v9, 31, v8
	v_lshl_add_u64 v[6:7], v[4:5], 0, v[6:7]
	v_lshlrev_b64 v[8:9], 13, v[8:9]
	v_lshl_add_u64 v[8:9], v[4:5], 0, v[8:9]
	global_load_dwordx4 v[118:121], v[6:7], off nt
	global_load_dwordx4 v[114:117], v[8:9], off nt
	v_or_b32_e32 v6, 32, v2
	v_ashrrev_i32_e32 v7, 31, v6
	v_or_b32_e32 v8, 40, v2
	v_lshlrev_b64 v[6:7], 13, v[6:7]
	v_ashrrev_i32_e32 v9, 31, v8
	v_lshl_add_u64 v[6:7], v[4:5], 0, v[6:7]
	v_lshlrev_b64 v[8:9], 13, v[8:9]
	v_lshl_add_u64 v[8:9], v[4:5], 0, v[8:9]
	global_load_dwordx4 v[110:113], v[6:7], off nt
	global_load_dwordx4 v[106:109], v[8:9], off nt
	v_or_b32_e32 v6, 48, v2
	v_ashrrev_i32_e32 v7, 31, v6
	v_or_b32_e32 v8, 56, v2
	v_lshlrev_b64 v[6:7], 13, v[6:7]
	v_ashrrev_i32_e32 v9, 31, v8
	v_lshl_add_u64 v[6:7], v[4:5], 0, v[6:7]
	v_lshlrev_b64 v[8:9], 13, v[8:9]
	v_lshl_add_u64 v[8:9], v[4:5], 0, v[8:9]
	global_load_dwordx4 v[94:97], v[6:7], off nt
	global_load_dwordx4 v[82:85], v[8:9], off nt
	v_or_b32_e32 v6, 64, v2
	v_ashrrev_i32_e32 v7, 31, v6
	v_or_b32_e32 v8, 0x48, v2
	v_lshlrev_b64 v[6:7], 13, v[6:7]
	v_ashrrev_i32_e32 v9, 31, v8
	v_lshl_add_u64 v[6:7], v[4:5], 0, v[6:7]
	v_lshlrev_b64 v[8:9], 13, v[8:9]
	v_lshl_add_u64 v[8:9], v[4:5], 0, v[8:9]
	global_load_dwordx4 v[70:73], v[6:7], off nt
	global_load_dwordx4 v[58:61], v[8:9], off nt
	v_or_b32_e32 v6, 0x50, v2
	v_ashrrev_i32_e32 v7, 31, v6
	v_or_b32_e32 v8, 0x58, v2
	v_lshlrev_b64 v[6:7], 13, v[6:7]
	v_ashrrev_i32_e32 v9, 31, v8
	v_lshl_add_u64 v[6:7], v[4:5], 0, v[6:7]
	v_lshlrev_b64 v[8:9], 13, v[8:9]
	v_lshl_add_u64 v[8:9], v[4:5], 0, v[8:9]
	global_load_dwordx4 v[54:57], v[6:7], off nt
	global_load_dwordx4 v[34:37], v[8:9], off nt
	v_or_b32_e32 v6, 0x60, v2
	v_ashrrev_i32_e32 v7, 31, v6
	v_or_b32_e32 v8, 0x68, v2
	v_lshlrev_b64 v[6:7], 13, v[6:7]
	v_ashrrev_i32_e32 v9, 31, v8
	v_lshl_add_u64 v[6:7], v[4:5], 0, v[6:7]
	v_lshlrev_b64 v[8:9], 13, v[8:9]
	v_lshl_add_u64 v[8:9], v[4:5], 0, v[8:9]
	global_load_dwordx4 v[30:33], v[6:7], off nt
	global_load_dwordx4 v[18:21], v[8:9], off nt
	v_or_b32_e32 v6, 0x70, v2
	v_ashrrev_i32_e32 v7, 31, v6
	v_or_b32_e32 v2, 0x78, v2
	v_lshlrev_b64 v[6:7], 13, v[6:7]
	v_ashrrev_i32_e32 v3, 31, v2
	v_lshl_add_u64 v[14:15], v[4:5], 0, v[6:7]
	v_lshlrev_b64 v[2:3], 13, v[2:3]
	v_lshl_add_u64 v[16:17], v[4:5], 0, v[2:3]
	global_load_dwordx4 v[6:9], v[14:15], off nt
	global_load_dwordx4 v[2:5], v[16:17], off nt
	v_and_b32_e32 v10, 63, v10
	v_lshlrev_b32_e32 v10, 4, v10
	v_mul_u32_u24_e32 v11, 0x90, v12
	v_and_b32_e32 v140, 0x70, v10
	s_mov_b64 s[6:7], 0x18000000
	v_add3_u32 v144, s9, v11, v1
	v_add_u32_e32 v11, s9, v140
	v_mul_u32_u24_e32 v13, 0x90, v1
	v_lshl_add_u64 v[138:139], v[132:133], 0, s[6:7]
	v_mov_b32_e32 v141, v137
	v_and_b32_e32 v145, 0x80, v10
	v_or_b32_e32 v146, 8, v1
	v_or_b32_e32 v147, 16, v1
	v_or_b32_e32 v148, 24, v1
	v_lshlrev_b32_e32 v136, 2, v12
	v_add_u32_e32 v149, v11, v13
	s_waitcnt vmcnt(0)
	s_branch .LBB0_114
.LBB0_113:
	v_mul_f32_e32 v126, 0x42800000, v126
	v_mul_f32_e32 v127, 0x42800000, v127
	v_mov_b32_e32 v150, 0
	v_cvt_pk_fp8_f32 v150, v126, v127
	v_mul_f32_e32 v126, 0x42800000, v128
	v_mul_f32_e32 v127, 0x42800000, v129
	v_mul_f32_e32 v122, 0x42800000, v122
	v_cvt_pk_fp8_f32 v150, v126, v127 op_sel:[0,0,1]
	v_mul_f32_e32 v123, 0x42800000, v123
	v_mov_b32_e32 v127, 0
	v_cvt_pk_fp8_f32 v127, v122, v123
	v_mul_f32_e32 v122, 0x42800000, v124
	v_mul_f32_e32 v123, 0x42800000, v125
	v_mul_f32_e32 v118, 0x42800000, v118
	v_cvt_pk_fp8_f32 v127, v122, v123 op_sel:[0,0,1]
	v_mul_f32_e32 v119, 0x42800000, v119
	v_mov_b32_e32 v123, 0
	v_cvt_pk_fp8_f32 v123, v118, v119
	v_mul_f32_e32 v118, 0x42800000, v120
	v_mul_f32_e32 v119, 0x42800000, v121
	v_mul_f32_e32 v114, 0x42800000, v114
	v_cvt_pk_fp8_f32 v123, v118, v119 op_sel:[0,0,1]
	v_mul_f32_e32 v115, 0x42800000, v115
	v_mov_b32_e32 v119, 0
	v_cvt_pk_fp8_f32 v119, v114, v115
	v_mul_f32_e32 v114, 0x42800000, v116
	v_mul_f32_e32 v115, 0x42800000, v117
	v_mul_f32_e32 v110, 0x42800000, v110
	v_cvt_pk_fp8_f32 v119, v114, v115 op_sel:[0,0,1]
	v_mul_f32_e32 v111, 0x42800000, v111
	v_mov_b32_e32 v115, 0
	v_cvt_pk_fp8_f32 v115, v110, v111
	v_mul_f32_e32 v110, 0x42800000, v112
	v_mul_f32_e32 v111, 0x42800000, v113
	v_mul_f32_e32 v106, 0x42800000, v106
	v_cvt_pk_fp8_f32 v115, v110, v111 op_sel:[0,0,1]
	v_mul_f32_e32 v107, 0x42800000, v107
	v_mov_b32_e32 v111, 0
	v_cvt_pk_fp8_f32 v111, v106, v107
	v_mul_f32_e32 v106, 0x42800000, v108
	v_mul_f32_e32 v107, 0x42800000, v109
	v_mul_f32_e32 v94, 0x42800000, v94
	v_cvt_pk_fp8_f32 v111, v106, v107 op_sel:[0,0,1]
	v_mul_f32_e32 v95, 0x42800000, v95
	v_mov_b32_e32 v107, 0
	v_cvt_pk_fp8_f32 v107, v94, v95
	v_mul_f32_e32 v94, 0x42800000, v96
	v_mul_f32_e32 v95, 0x42800000, v97
	v_mul_f32_e32 v82, 0x42800000, v82
	v_cvt_pk_fp8_f32 v107, v94, v95 op_sel:[0,0,1]
	v_mul_f32_e32 v83, 0x42800000, v83
	v_mov_b32_e32 v95, 0
	v_cvt_pk_fp8_f32 v95, v82, v83
	v_mul_f32_e32 v82, 0x42800000, v84
	v_mul_f32_e32 v83, 0x42800000, v85
	v_mul_f32_e32 v70, 0x42800000, v70
	v_cvt_pk_fp8_f32 v95, v82, v83 op_sel:[0,0,1]
	v_mul_f32_e32 v71, 0x42800000, v71
	v_mov_b32_e32 v83, 0
	v_cvt_pk_fp8_f32 v83, v70, v71
	v_mul_f32_e32 v70, 0x42800000, v72
	v_mul_f32_e32 v71, 0x42800000, v73
	v_mul_f32_e32 v58, 0x42800000, v58
	v_cvt_pk_fp8_f32 v83, v70, v71 op_sel:[0,0,1]
	v_mul_f32_e32 v59, 0x42800000, v59
	v_mov_b32_e32 v71, 0
	v_cvt_pk_fp8_f32 v71, v58, v59
	v_mul_f32_e32 v58, 0x42800000, v60
	v_mul_f32_e32 v59, 0x42800000, v61
	v_mul_f32_e32 v54, 0x42800000, v54
	v_cvt_pk_fp8_f32 v71, v58, v59 op_sel:[0,0,1]
	v_mul_f32_e32 v55, 0x42800000, v55
	v_mov_b32_e32 v59, 0
	v_cvt_pk_fp8_f32 v59, v54, v55
	v_mul_f32_e32 v54, 0x42800000, v56
	v_mul_f32_e32 v55, 0x42800000, v57
	v_mul_f32_e32 v34, 0x42800000, v34
	v_cvt_pk_fp8_f32 v59, v54, v55 op_sel:[0,0,1]
	v_mul_f32_e32 v35, 0x42800000, v35
	v_mov_b32_e32 v55, 0
	v_cvt_pk_fp8_f32 v55, v34, v35
	v_mul_f32_e32 v34, 0x42800000, v36
	v_mul_f32_e32 v35, 0x42800000, v37
	v_mul_f32_e32 v30, 0x42800000, v30
	v_cvt_pk_fp8_f32 v55, v34, v35 op_sel:[0,0,1]
	v_mul_f32_e32 v31, 0x42800000, v31
	v_mov_b32_e32 v35, 0
	v_cvt_pk_fp8_f32 v35, v30, v31
	v_mul_f32_e32 v30, 0x42800000, v32
	v_mul_f32_e32 v31, 0x42800000, v33
	v_mul_f32_e32 v18, 0x42800000, v18
	v_cvt_pk_fp8_f32 v35, v30, v31 op_sel:[0,0,1]
	v_mul_f32_e32 v19, 0x42800000, v19
	v_mov_b32_e32 v31, 0
	v_cvt_pk_fp8_f32 v31, v18, v19
	v_lshrrev_b32_e32 v126, 8, v150
	v_lshrrev_b32_e32 v122, 24, v150
	v_mul_f32_e32 v18, 0x42800000, v20
	v_mul_f32_e32 v19, 0x42800000, v21
	ds_write_b8 v144, v150
	ds_write_b8 v144, v126 offset:144
	ds_write_b8_d16_hi v144, v150 offset:288
	ds_write_b8 v144, v122 offset:432
	ds_write_b8 v144, v127 offset:8
	v_lshrrev_b32_e32 v122, 8, v127
	v_lshrrev_b32_e32 v118, 24, v127
	v_cvt_pk_fp8_f32 v31, v18, v19 op_sel:[0,0,1]
	v_mul_f32_e32 v6, 0x42800000, v6
	v_mul_f32_e32 v7, 0x42800000, v7
	v_mov_b32_e32 v19, 0
	ds_write_b8 v144, v122 offset:152
	ds_write_b8_d16_hi v144, v127 offset:296
	ds_write_b8 v144, v118 offset:440
	ds_write_b8 v144, v123 offset:16
	v_lshrrev_b32_e32 v118, 8, v123
	v_lshrrev_b32_e32 v114, 24, v123
	v_cvt_pk_fp8_f32 v19, v6, v7
	ds_write_b8 v144, v118 offset:160
	ds_write_b8_d16_hi v144, v123 offset:304
	ds_write_b8 v144, v114 offset:448
	ds_write_b8 v144, v119 offset:24
	v_lshrrev_b32_e32 v114, 8, v119
	v_lshrrev_b32_e32 v110, 24, v119
	ds_write_b8 v144, v114 offset:168
	ds_write_b8_d16_hi v144, v119 offset:312
	ds_write_b8 v144, v110 offset:456
	ds_write_b8 v144, v115 offset:32
	v_lshrrev_b32_e32 v110, 8, v115
	v_lshrrev_b32_e32 v106, 24, v115
	ds_write_b8 v144, v110 offset:176
	ds_write_b8_d16_hi v144, v115 offset:320
	ds_write_b8 v144, v106 offset:464
	ds_write_b8 v144, v111 offset:40
	v_lshrrev_b32_e32 v106, 8, v111
	v_lshrrev_b32_e32 v94, 24, v111
	v_mul_f32_e32 v6, 0x42800000, v8
	v_mul_f32_e32 v7, 0x42800000, v9
	ds_write_b8 v144, v106 offset:184
	ds_write_b8_d16_hi v144, v111 offset:328
	ds_write_b8 v144, v94 offset:472
	ds_write_b8 v144, v107 offset:48
	v_lshrrev_b32_e32 v94, 8, v107
	v_lshrrev_b32_e32 v82, 24, v107
	v_cvt_pk_fp8_f32 v19, v6, v7 op_sel:[0,0,1]
	v_mul_f32_e32 v2, 0x42800000, v2
	v_mul_f32_e32 v3, 0x42800000, v3
	v_mov_b32_e32 v7, 0
	s_ashr_i32 s9, s8, 31
	ds_write_b8 v144, v94 offset:192
	ds_write_b8_d16_hi v144, v107 offset:336
	ds_write_b8 v144, v82 offset:480
	ds_write_b8 v144, v95 offset:56
	v_lshrrev_b32_e32 v82, 8, v95
	v_lshrrev_b32_e32 v70, 24, v95
	v_cvt_pk_fp8_f32 v7, v2, v3
	s_lshr_b32 s9, s9, 23
	ds_write_b8 v144, v82 offset:200
	ds_write_b8_d16_hi v144, v95 offset:344
	ds_write_b8 v144, v70 offset:488
	ds_write_b8 v144, v83 offset:64
	v_lshrrev_b32_e32 v70, 8, v83
	v_lshrrev_b32_e32 v58, 24, v83
	s_add_i32 s9, s8, s9
	ds_write_b8 v144, v70 offset:208
	ds_write_b8_d16_hi v144, v83 offset:352
	ds_write_b8 v144, v58 offset:496
	ds_write_b8 v144, v71 offset:72
	v_lshrrev_b32_e32 v58, 8, v71
	v_lshrrev_b32_e32 v54, 24, v71
	s_ashr_i32 s12, s9, 9
	s_and_b32 s9, s9, 0xfffffe00
	ds_write_b8 v144, v58 offset:216
	ds_write_b8_d16_hi v144, v71 offset:360
	ds_write_b8 v144, v54 offset:504
	ds_write_b8 v144, v59 offset:80
	v_lshrrev_b32_e32 v54, 8, v59
	v_lshrrev_b32_e32 v34, 24, v59
	v_mul_f32_e32 v2, 0x42800000, v4
	v_mul_f32_e32 v3, 0x42800000, v5
	s_sub_i32 s9, s8, s9
	ds_write_b8 v144, v54 offset:224
	ds_write_b8_d16_hi v144, v59 offset:368
	ds_write_b8 v144, v34 offset:512
	ds_write_b8 v144, v55 offset:88
	v_lshrrev_b32_e32 v34, 8, v55
	v_lshrrev_b32_e32 v30, 24, v55
	v_cvt_pk_fp8_f32 v7, v2, v3 op_sel:[0,0,1]
	s_ashr_i32 s8, s9, 31
	ds_write_b8 v144, v34 offset:232
	ds_write_b8_d16_hi v144, v55 offset:376
	ds_write_b8 v144, v30 offset:520
	ds_write_b8 v144, v35 offset:96
	v_lshrrev_b32_e32 v30, 8, v35
	v_lshrrev_b32_e32 v18, 24, v35
	s_lshr_b32 s8, s8, 26
	ds_write_b8 v144, v30 offset:240
	ds_write_b8_d16_hi v144, v35 offset:384
	ds_write_b8 v144, v18 offset:528
	ds_write_b8 v144, v31 offset:104
	v_lshrrev_b32_e32 v18, 8, v31
	v_lshrrev_b32_e32 v6, 24, v31
	s_add_i32 s11, s9, s8
	ds_write_b8 v144, v18 offset:248
	ds_write_b8_d16_hi v144, v31 offset:392
	ds_write_b8 v144, v6 offset:536
	ds_write_b8 v144, v19 offset:112
	v_lshrrev_b32_e32 v6, 8, v19
	v_lshrrev_b32_e32 v2, 24, v19
	s_lshl_b32 s8, s11, 1
	ds_write_b8 v144, v6 offset:256
	ds_write_b8_d16_hi v144, v19 offset:400
	ds_write_b8 v144, v2 offset:544
	ds_write_b8 v144, v7 offset:120
	v_lshrrev_b32_e32 v2, 8, v7
	s_and_b32 s11, s11, 0x7ffffc0
	s_ashr_i32 s13, s12, 31
	ds_write_b8 v144, v2 offset:264
	ds_write_b8_d16_hi v144, v7 offset:408
	v_lshrrev_b32_e32 v2, 24, v7
	s_sub_i32 s9, s9, s11
	s_lshl_b64 s[12:13], s[12:13], 21
	s_and_b32 s8, s8, 0xffffff80
	ds_write_b8 v144, v2 offset:552
	s_lshl_b32 s11, s9, 5
	v_lshl_add_u64 v[142:143], v[138:139], 0, s[12:13]
	s_waitcnt lgkmcnt(0)
	s_ashr_i32 s9, s8, 31
	v_or_b32_e32 v6, s11, v1
	v_lshl_add_u64 v[2:3], v[142:143], 0, s[8:9]
	v_lshrrev_b32_e32 v6, 1, v6
	s_and_b32 s12, s11, 0xffffff00
	v_lshl_add_u64 v[18:19], v[2:3], 0, v[140:141]
	ds_read_b128 v[2:5], v149
	v_and_b32_e32 v6, 0x73, v6
	v_or3_b32 v6, v145, v6, s12
	v_ashrrev_i32_e32 v7, 31, v6
	v_lshlrev_b64 v[6:7], 10, v[6:7]
	v_lshl_add_u64 v[20:21], v[18:19], 0, v[6:7]
	ds_read_b128 v[6:9], v149 offset:1152
	s_waitcnt lgkmcnt(1)
	global_store_dwordx4 v[20:21], v[2:5], off nt
	s_waitcnt vmcnt(1)
	v_mov_b64_e32 v[30:31], v[90:91]
	v_mov_b64_e32 v[34:35], v[74:75]
	v_or_b32_e32 v2, s11, v146
	v_lshrrev_b32_e32 v2, 1, v2
	v_and_b32_e32 v2, 0x77, v2
	v_or3_b32 v2, v145, v2, s12
	v_ashrrev_i32_e32 v3, 31, v2
	v_lshlrev_b64 v[2:3], 10, v[2:3]
	v_lshl_add_u64 v[2:3], v[18:19], 0, v[2:3]
	s_waitcnt lgkmcnt(0)
	global_store_dwordx4 v[2:3], v[6:9], off nt
	ds_read_b128 v[2:5], v149 offset:2304
	v_mov_b64_e32 v[54:55], v[78:79]
	v_or_b32_e32 v6, s11, v147
	v_lshrrev_b32_e32 v6, 1, v6
	v_and_b32_e32 v6, 0x7b, v6
	v_or3_b32 v6, v145, v6, s12
	v_ashrrev_i32_e32 v7, 31, v6
	v_lshlrev_b64 v[6:7], 10, v[6:7]
	v_lshl_add_u64 v[20:21], v[18:19], 0, v[6:7]
	ds_read_b128 v[6:9], v149 offset:3456
	s_waitcnt lgkmcnt(1)
	global_store_dwordx4 v[20:21], v[2:5], off nt
	v_mov_b64_e32 v[58:59], v[62:63]
	v_mov_b64_e32 v[72:73], v[68:69]
	v_or_b32_e32 v2, s11, v148
	v_bfe_u32 v2, v2, 1, 7
	v_or3_b32 v2, v145, v2, s12
	v_ashrrev_i32_e32 v3, 31, v2
	v_lshlrev_b64 v[2:3], 10, v[2:3]
	v_lshl_add_u64 v[2:3], v[18:19], 0, v[2:3]
	s_waitcnt lgkmcnt(0)
	global_store_dwordx4 v[2:3], v[6:9], off nt
	s_waitcnt lgkmcnt(0)
	v_mov_b64_e32 v[2:3], v[98:99]
	v_mov_b64_e32 v[18:19], v[86:87]
	v_mov_b64_e32 v[6:7], v[102:103]
	v_mov_b64_e32 v[84:85], v[48:49]
	v_mov_b64_e32 v[96:97], v[52:53]
	v_mov_b64_e32 v[108:109], v[40:41]
	v_mov_b64_e32 v[112:113], v[44:45]
	v_mov_b64_e32 v[116:117], v[24:25]
	v_mov_b64_e32 v[120:121], v[28:29]
	v_mov_b64_e32 v[124:125], v[12:13]
	v_mov_b64_e32 v[128:129], v[16:17]
	s_andn2_b64 vcc, exec, s[6:7]
	v_mov_b64_e32 v[4:5], v[100:101]
	v_mov_b64_e32 v[8:9], v[104:105]
	v_mov_b64_e32 v[20:21], v[88:89]
	v_mov_b64_e32 v[32:33], v[92:93]
	v_mov_b64_e32 v[36:37], v[76:77]
	v_mov_b64_e32 v[56:57], v[80:81]
	v_mov_b64_e32 v[60:61], v[64:65]
	v_mov_b64_e32 v[70:71], v[66:67]
	v_mov_b64_e32 v[82:83], v[46:47]
	v_mov_b64_e32 v[94:95], v[50:51]
	v_mov_b64_e32 v[106:107], v[38:39]
	v_mov_b64_e32 v[110:111], v[42:43]
	v_mov_b64_e32 v[114:115], v[22:23]
	v_mov_b64_e32 v[118:119], v[26:27]
	v_mov_b64_e32 v[122:123], v[10:11]
	v_mov_b64_e32 v[126:127], v[14:15]
	s_mov_b32 s8, s10
	s_cbranch_vccz .LBB0_116

.LBB0_116:
	s_mov_b32 s4, 22
	v_mov_b32_e32 v14, v0
	s_nop 0
	v_readfirstlane_b32 s5, v14
	s_ashr_i32 s6, s5, 6
	s_add_i32 s8, s6, s3
	s_cmpk_gt_i32 s8, 0x7fff
	s_cbranch_scc1 .LBB0_121
	s_ashr_i32 s5, s4, 31
	s_lshl_b64 s[4:5], s[4:5], 3
	s_add_u32 s4, s94, s4
	s_addc_u32 s5, s95, s5
	s_lshl_b32 s6, s6, 14
	s_add_i32 s9, s6, 0
	s_ashr_i32 s6, s8, 31
	s_load_dwordx2 s[4:5], s[4:5], 0x0
	s_lshr_b32 s6, s6, 24
	s_add_i32 s10, s8, s6
	s_ashr_i32 s6, s10, 8
	s_ashr_i32 s7, s6, 31
	s_lshl_b64 s[6:7], s[6:7], 22
	s_waitcnt lgkmcnt(0)
	s_add_u32 s11, s4, s6
	s_addc_u32 s12, s5, s7
	s_and_b32 s6, s10, 0xffffff00
	s_sub_i32 s6, s8, s6
	s_ashr_i32 s7, s6, 31
	s_lshr_b32 s7, s7, 27
	s_add_i32 s7, s6, s7
	s_and_b32 s10, s7, 0x7ffffe0
	s_sub_i32 s6, s6, s10
	s_lshl_b32 s7, s7, 2
	s_and_b32 s7, s7, 0xffffff80
	s_lshl_b32 s6, s6, 5
	v_bfe_u32 v1, v14, 3, 3
	s_waitcnt vmcnt(0)
	v_or_b32_e32 v2, s7, v1
	s_ashr_i32 s7, s6, 31
	s_lshl_b64 s[6:7], s[6:7], 2
	v_lshlrev_b32_e32 v3, 2, v14
	s_add_u32 s6, s11, s6
	v_and_b32_e32 v16, 28, v3
	s_addc_u32 s7, s12, s7
	v_mov_b32_e32 v137, 0
	v_lshlrev_b32_e32 v136, 2, v16
	v_ashrrev_i32_e32 v3, 31, v2
	v_or_b32_e32 v8, 8, v2
	v_lshl_add_u64 v[4:5], s[6:7], 0, v[136:137]
	v_lshlrev_b64 v[6:7], 12, v[2:3]
	v_ashrrev_i32_e32 v9, 31, v8
	v_lshl_add_u64 v[6:7], v[4:5], 0, v[6:7]
	v_lshlrev_b64 v[8:9], 12, v[8:9]
	v_lshl_add_u64 v[8:9], v[4:5], 0, v[8:9]
	global_load_dwordx4 v[126:129], v[6:7], off nt
	global_load_dwordx4 v[122:125], v[8:9], off nt
	v_or_b32_e32 v6, 16, v2
	v_ashrrev_i32_e32 v7, 31, v6
	v_or_b32_e32 v8, 24, v2
	v_lshlrev_b64 v[6:7], 12, v[6:7]
	v_ashrrev_i32_e32 v9, 31, v8
	v_lshl_add_u64 v[6:7], v[4:5], 0, v[6:7]
	v_lshlrev_b64 v[8:9], 12, v[8:9]
	v_lshl_add_u64 v[8:9], v[4:5], 0, v[8:9]
	global_load_dwordx4 v[118:121], v[6:7], off nt
	global_load_dwordx4 v[114:117], v[8:9], off nt
	v_or_b32_e32 v6, 32, v2
	v_ashrrev_i32_e32 v7, 31, v6
	v_or_b32_e32 v8, 40, v2
	v_lshlrev_b64 v[6:7], 12, v[6:7]
	v_ashrrev_i32_e32 v9, 31, v8
	v_lshl_add_u64 v[6:7], v[4:5], 0, v[6:7]
	v_lshlrev_b64 v[8:9], 12, v[8:9]
	v_lshl_add_u64 v[8:9], v[4:5], 0, v[8:9]
	global_load_dwordx4 v[110:113], v[6:7], off nt
	global_load_dwordx4 v[98:101], v[8:9], off nt
	v_or_b32_e32 v6, 48, v2
	v_ashrrev_i32_e32 v7, 31, v6
	v_or_b32_e32 v8, 56, v2
	v_lshlrev_b64 v[6:7], 12, v[6:7]
	v_ashrrev_i32_e32 v9, 31, v8
	v_lshl_add_u64 v[6:7], v[4:5], 0, v[6:7]
	v_lshlrev_b64 v[8:9], 12, v[8:9]
	v_lshl_add_u64 v[8:9], v[4:5], 0, v[8:9]
	global_load_dwordx4 v[86:89], v[6:7], off nt
	global_load_dwordx4 v[74:77], v[8:9], off nt
	v_or_b32_e32 v6, 64, v2
	v_ashrrev_i32_e32 v7, 31, v6
	v_or_b32_e32 v8, 0x48, v2
	v_lshlrev_b64 v[6:7], 12, v[6:7]
	v_ashrrev_i32_e32 v9, 31, v8
	v_lshl_add_u64 v[6:7], v[4:5], 0, v[6:7]
	v_lshlrev_b64 v[8:9], 12, v[8:9]
	v_lshl_add_u64 v[8:9], v[4:5], 0, v[8:9]
	global_load_dwordx4 v[70:73], v[6:7], off nt
	global_load_dwordx4 v[50:53], v[8:9], off nt
	v_or_b32_e32 v6, 0x50, v2
	v_ashrrev_i32_e32 v7, 31, v6
	v_or_b32_e32 v8, 0x58, v2
	v_lshlrev_b64 v[6:7], 12, v[6:7]
	v_ashrrev_i32_e32 v9, 31, v8
	v_lshl_add_u64 v[6:7], v[4:5], 0, v[6:7]
	v_lshlrev_b64 v[8:9], 12, v[8:9]
	v_lshl_add_u64 v[8:9], v[4:5], 0, v[8:9]
	global_load_dwordx4 v[46:49], v[6:7], off nt
	global_load_dwordx4 v[34:37], v[8:9], off nt
	v_or_b32_e32 v6, 0x60, v2
	v_ashrrev_i32_e32 v7, 31, v6
	v_or_b32_e32 v8, 0x68, v2
	v_lshlrev_b64 v[6:7], 12, v[6:7]
	v_ashrrev_i32_e32 v9, 31, v8
	v_lshl_add_u64 v[6:7], v[4:5], 0, v[6:7]
	v_lshlrev_b64 v[8:9], 12, v[8:9]
	v_lshl_add_u64 v[8:9], v[4:5], 0, v[8:9]
	global_load_dwordx4 v[22:25], v[6:7], off nt
	global_load_dwordx4 v[10:13], v[8:9], off nt
	v_or_b32_e32 v6, 0x70, v2
	v_ashrrev_i32_e32 v7, 31, v6
	v_or_b32_e32 v2, 0x78, v2
	v_lshlrev_b64 v[6:7], 12, v[6:7]
	v_ashrrev_i32_e32 v3, 31, v2
	v_lshl_add_u64 v[18:19], v[4:5], 0, v[6:7]
	v_lshlrev_b64 v[2:3], 12, v[2:3]
	v_lshl_add_u64 v[20:21], v[4:5], 0, v[2:3]
	global_load_dwordx4 v[6:9], v[18:19], off nt
	global_load_dwordx4 v[2:5], v[20:21], off nt
	v_lshlrev_b32_e32 v14, 4, v14
	v_mul_u32_u24_e32 v15, 0x90, v16
	v_and_b32_e32 v138, 0x70, v14
	s_mov_b64 s[6:7], 0x38000000
	v_add3_u32 v142, s9, v15, v1
	v_add_u32_e32 v14, s9, v138
	v_mul_u32_u24_e32 v15, 0x90, v1
	v_lshl_add_u64 v[132:133], v[132:133], 0, s[6:7]
	v_or_b32_e32 v143, 8, v1
	v_or_b32_e32 v144, 16, v1
	v_or_b32_e32 v145, 24, v1
	v_mov_b32_e32 v139, v137
	v_lshlrev_b32_e32 v136, 2, v16
	v_add_u32_e32 v146, v14, v15
	s_waitcnt vmcnt(0)
	s_branch .LBB0_119
.LBB0_118:
	v_mul_f32_e32 v126, 0x42800000, v126
	v_mul_f32_e32 v127, 0x42800000, v127
	v_mov_b32_e32 v147, 0
	v_cvt_pk_fp8_f32 v147, v126, v127
	v_mul_f32_e32 v126, 0x42800000, v128
	v_mul_f32_e32 v127, 0x42800000, v129
	v_mul_f32_e32 v122, 0x42800000, v122
	v_cvt_pk_fp8_f32 v147, v126, v127 op_sel:[0,0,1]
	v_mul_f32_e32 v123, 0x42800000, v123
	v_mov_b32_e32 v127, 0
	v_cvt_pk_fp8_f32 v127, v122, v123
	v_mul_f32_e32 v122, 0x42800000, v124
	v_mul_f32_e32 v123, 0x42800000, v125
	v_mul_f32_e32 v118, 0x42800000, v118
	v_cvt_pk_fp8_f32 v127, v122, v123 op_sel:[0,0,1]
	v_mul_f32_e32 v119, 0x42800000, v119
	v_mov_b32_e32 v123, 0
	v_cvt_pk_fp8_f32 v123, v118, v119
	v_mul_f32_e32 v118, 0x42800000, v120
	v_mul_f32_e32 v119, 0x42800000, v121
	v_mul_f32_e32 v114, 0x42800000, v114
	v_cvt_pk_fp8_f32 v123, v118, v119 op_sel:[0,0,1]
	v_mul_f32_e32 v115, 0x42800000, v115
	v_mov_b32_e32 v119, 0
	v_cvt_pk_fp8_f32 v119, v114, v115
	v_mul_f32_e32 v114, 0x42800000, v116
	v_mul_f32_e32 v115, 0x42800000, v117
	v_mul_f32_e32 v110, 0x42800000, v110
	v_cvt_pk_fp8_f32 v119, v114, v115 op_sel:[0,0,1]
	v_mul_f32_e32 v111, 0x42800000, v111
	v_mov_b32_e32 v115, 0
	v_cvt_pk_fp8_f32 v115, v110, v111
	v_mul_f32_e32 v110, 0x42800000, v112
	v_mul_f32_e32 v111, 0x42800000, v113
	v_mul_f32_e32 v98, 0x42800000, v98
	v_cvt_pk_fp8_f32 v115, v110, v111 op_sel:[0,0,1]
	v_mul_f32_e32 v99, 0x42800000, v99
	v_mov_b32_e32 v111, 0
	v_cvt_pk_fp8_f32 v111, v98, v99
	v_mul_f32_e32 v98, 0x42800000, v100
	v_mul_f32_e32 v99, 0x42800000, v101
	v_mul_f32_e32 v86, 0x42800000, v86
	v_cvt_pk_fp8_f32 v111, v98, v99 op_sel:[0,0,1]
	v_mul_f32_e32 v87, 0x42800000, v87
	v_mov_b32_e32 v99, 0
	v_cvt_pk_fp8_f32 v99, v86, v87
	v_mul_f32_e32 v86, 0x42800000, v88
	v_mul_f32_e32 v87, 0x42800000, v89
	v_mul_f32_e32 v74, 0x42800000, v74
	v_cvt_pk_fp8_f32 v99, v86, v87 op_sel:[0,0,1]
	v_mul_f32_e32 v75, 0x42800000, v75
	v_mov_b32_e32 v87, 0
	v_cvt_pk_fp8_f32 v87, v74, v75
	v_mul_f32_e32 v74, 0x42800000, v76
	v_mul_f32_e32 v75, 0x42800000, v77
	v_mul_f32_e32 v70, 0x42800000, v70
	v_cvt_pk_fp8_f32 v87, v74, v75 op_sel:[0,0,1]
	v_mul_f32_e32 v71, 0x42800000, v71
	v_mov_b32_e32 v75, 0
	v_cvt_pk_fp8_f32 v75, v70, v71
	v_mul_f32_e32 v70, 0x42800000, v72
	v_mul_f32_e32 v71, 0x42800000, v73
	v_mul_f32_e32 v50, 0x42800000, v50
	v_cvt_pk_fp8_f32 v75, v70, v71 op_sel:[0,0,1]
	v_mul_f32_e32 v51, 0x42800000, v51
	v_mov_b32_e32 v71, 0
	v_cvt_pk_fp8_f32 v71, v50, v51
	v_mul_f32_e32 v50, 0x42800000, v52
	v_mul_f32_e32 v51, 0x42800000, v53
	v_mul_f32_e32 v46, 0x42800000, v46
	v_cvt_pk_fp8_f32 v71, v50, v51 op_sel:[0,0,1]
	v_mul_f32_e32 v47, 0x42800000, v47
	v_mov_b32_e32 v51, 0
	v_cvt_pk_fp8_f32 v51, v46, v47
	v_mul_f32_e32 v46, 0x42800000, v48
	v_mul_f32_e32 v47, 0x42800000, v49
	v_mul_f32_e32 v34, 0x42800000, v34
	v_cvt_pk_fp8_f32 v51, v46, v47 op_sel:[0,0,1]
	v_mul_f32_e32 v35, 0x42800000, v35
	v_mov_b32_e32 v47, 0
	v_cvt_pk_fp8_f32 v47, v34, v35
	v_mul_f32_e32 v34, 0x42800000, v36
	v_mul_f32_e32 v35, 0x42800000, v37
	v_mul_f32_e32 v22, 0x42800000, v22
	v_cvt_pk_fp8_f32 v47, v34, v35 op_sel:[0,0,1]
	v_mul_f32_e32 v23, 0x42800000, v23
	v_mov_b32_e32 v35, 0
	v_cvt_pk_fp8_f32 v35, v22, v23
	v_mul_f32_e32 v22, 0x42800000, v24
	v_mul_f32_e32 v23, 0x42800000, v25
	v_mul_f32_e32 v10, 0x42800000, v10
	v_cvt_pk_fp8_f32 v35, v22, v23 op_sel:[0,0,1]
	v_mul_f32_e32 v11, 0x42800000, v11
	v_mov_b32_e32 v23, 0
	v_cvt_pk_fp8_f32 v23, v10, v11
	v_lshrrev_b32_e32 v126, 8, v147
	v_lshrrev_b32_e32 v122, 24, v147
	v_mul_f32_e32 v10, 0x42800000, v12
	v_mul_f32_e32 v11, 0x42800000, v13
	ds_write_b8 v142, v147
	ds_write_b8 v142, v126 offset:144
	ds_write_b8_d16_hi v142, v147 offset:288
	ds_write_b8 v142, v122 offset:432
	ds_write_b8 v142, v127 offset:8
	v_lshrrev_b32_e32 v122, 8, v127
	v_lshrrev_b32_e32 v118, 24, v127
	v_cvt_pk_fp8_f32 v23, v10, v11 op_sel:[0,0,1]
	v_mul_f32_e32 v6, 0x42800000, v6
	v_mul_f32_e32 v7, 0x42800000, v7
	v_mov_b32_e32 v11, 0
	ds_write_b8 v142, v122 offset:152
	ds_write_b8_d16_hi v142, v127 offset:296
	ds_write_b8 v142, v118 offset:440
	ds_write_b8 v142, v123 offset:16
	v_lshrrev_b32_e32 v118, 8, v123
	v_lshrrev_b32_e32 v114, 24, v123
	v_cvt_pk_fp8_f32 v11, v6, v7
	ds_write_b8 v142, v118 offset:160
	ds_write_b8_d16_hi v142, v123 offset:304
	ds_write_b8 v142, v114 offset:448
	ds_write_b8 v142, v119 offset:24
	v_lshrrev_b32_e32 v114, 8, v119
	v_lshrrev_b32_e32 v110, 24, v119
	ds_write_b8 v142, v114 offset:168
	ds_write_b8_d16_hi v142, v119 offset:312
	ds_write_b8 v142, v110 offset:456
	ds_write_b8 v142, v115 offset:32
	v_lshrrev_b32_e32 v110, 8, v115
	v_lshrrev_b32_e32 v98, 24, v115
	ds_write_b8 v142, v110 offset:176
	ds_write_b8_d16_hi v142, v115 offset:320
	ds_write_b8 v142, v98 offset:464
	ds_write_b8 v142, v111 offset:40
	v_lshrrev_b32_e32 v98, 8, v111
	v_lshrrev_b32_e32 v86, 24, v111
	v_mul_f32_e32 v6, 0x42800000, v8
	v_mul_f32_e32 v7, 0x42800000, v9
	ds_write_b8 v142, v98 offset:184
	ds_write_b8_d16_hi v142, v111 offset:328
	ds_write_b8 v142, v86 offset:472
	ds_write_b8 v142, v99 offset:48
	v_lshrrev_b32_e32 v86, 8, v99
	v_lshrrev_b32_e32 v74, 24, v99
	v_cvt_pk_fp8_f32 v11, v6, v7 op_sel:[0,0,1]
	v_mul_f32_e32 v2, 0x42800000, v2
	v_mul_f32_e32 v3, 0x42800000, v3
	v_mov_b32_e32 v7, 0
	ds_write_b8 v142, v86 offset:192
	ds_write_b8_d16_hi v142, v99 offset:336
	ds_write_b8 v142, v74 offset:480
	ds_write_b8 v142, v87 offset:56
	v_lshrrev_b32_e32 v74, 8, v87
	v_lshrrev_b32_e32 v70, 24, v87
	v_cvt_pk_fp8_f32 v7, v2, v3
	s_ashr_i32 s9, s8, 31
	ds_write_b8 v142, v74 offset:200
	ds_write_b8_d16_hi v142, v87 offset:344
	ds_write_b8 v142, v70 offset:488
	ds_write_b8 v142, v75 offset:64
	v_lshrrev_b32_e32 v70, 8, v75
	v_lshrrev_b32_e32 v50, 24, v75
	s_lshr_b32 s9, s9, 24
	ds_write_b8 v142, v70 offset:208
	ds_write_b8_d16_hi v142, v75 offset:352
	ds_write_b8 v142, v50 offset:496
	ds_write_b8 v142, v71 offset:72
	v_lshrrev_b32_e32 v50, 8, v71
	v_lshrrev_b32_e32 v46, 24, v71
	s_add_i32 s9, s8, s9
	ds_write_b8 v142, v50 offset:216
	ds_write_b8_d16_hi v142, v71 offset:360
	ds_write_b8 v142, v46 offset:504
	ds_write_b8 v142, v51 offset:80
	v_lshrrev_b32_e32 v46, 8, v51
	v_lshrrev_b32_e32 v34, 24, v51
	v_mul_f32_e32 v2, 0x42800000, v4
	v_mul_f32_e32 v3, 0x42800000, v5
	s_ashr_i32 s12, s9, 8
	s_and_b32 s9, s9, 0xffffff00
	ds_write_b8 v142, v46 offset:224
	ds_write_b8_d16_hi v142, v51 offset:368
	ds_write_b8 v142, v34 offset:512
	ds_write_b8 v142, v47 offset:88
	v_lshrrev_b32_e32 v34, 8, v47
	v_lshrrev_b32_e32 v22, 24, v47
	v_cvt_pk_fp8_f32 v7, v2, v3 op_sel:[0,0,1]
	s_sub_i32 s9, s8, s9
	ds_write_b8 v142, v34 offset:232
	ds_write_b8_d16_hi v142, v47 offset:376
	ds_write_b8 v142, v22 offset:520
	ds_write_b8 v142, v35 offset:96
	v_lshrrev_b32_e32 v22, 8, v35
	v_lshrrev_b32_e32 v10, 24, v35
	s_ashr_i32 s8, s9, 31
	ds_write_b8 v142, v22 offset:240
	ds_write_b8_d16_hi v142, v35 offset:384
	ds_write_b8 v142, v10 offset:528
	ds_write_b8 v142, v23 offset:104
	v_lshrrev_b32_e32 v10, 8, v23
	v_lshrrev_b32_e32 v6, 24, v23
	s_lshr_b32 s8, s8, 27
	ds_write_b8 v142, v10 offset:248
	ds_write_b8_d16_hi v142, v23 offset:392
	ds_write_b8 v142, v6 offset:536
	ds_write_b8 v142, v11 offset:112
	v_lshrrev_b32_e32 v6, 8, v11
	v_lshrrev_b32_e32 v2, 24, v11
	s_add_i32 s11, s9, s8
	ds_write_b8 v142, v6 offset:256
	ds_write_b8_d16_hi v142, v11 offset:400
	ds_write_b8 v142, v2 offset:544
	ds_write_b8 v142, v7 offset:120
	v_lshrrev_b32_e32 v2, 8, v7
	s_ashr_i32 s13, s12, 31
	s_lshl_b32 s8, s11, 2
	ds_write_b8 v142, v2 offset:264
	ds_write_b8_d16_hi v142, v7 offset:408
	v_lshrrev_b32_e32 v2, 24, v7
	s_and_b32 s11, s11, 0x7ffffe0
	s_lshl_b64 s[12:13], s[12:13], 20
	s_and_b32 s8, s8, 0xffffff80
	ds_write_b8 v142, v2 offset:552
	s_sub_i32 s9, s9, s11
	v_lshl_add_u64 v[140:141], v[132:133], 0, s[12:13]
	s_lshl_b32 s11, s9, 5
	s_waitcnt lgkmcnt(0)
	s_ashr_i32 s9, s8, 31
	v_lshl_add_u64 v[2:3], v[140:141], 0, s[8:9]
	v_lshl_add_u64 v[10:11], v[2:3], 0, v[138:139]
	ds_read_b128 v[2:5], v146
	v_or_b32_e32 v6, s11, v1
	v_ashrrev_i32_e32 v7, 31, v6
	v_lshlrev_b64 v[6:7], 10, v[6:7]
	v_lshl_add_u64 v[12:13], v[10:11], 0, v[6:7]
	ds_read_b128 v[6:9], v146 offset:1152
	s_waitcnt lgkmcnt(1)
	global_store_dwordx4 v[12:13], v[2:5], off nt
	s_waitcnt vmcnt(1)
	v_mov_b64_e32 v[22:23], v[94:95]
	v_mov_b64_e32 v[34:35], v[78:79]
	v_or_b32_e32 v2, s11, v143
	v_ashrrev_i32_e32 v3, 31, v2
	v_lshlrev_b64 v[2:3], 10, v[2:3]
	v_lshl_add_u64 v[2:3], v[10:11], 0, v[2:3]
	s_waitcnt lgkmcnt(0)
	global_store_dwordx4 v[2:3], v[6:9], off nt
	ds_read_b128 v[2:5], v146 offset:2304
	v_mov_b64_e32 v[46:47], v[82:83]
	v_or_b32_e32 v6, s11, v144
	v_ashrrev_i32_e32 v7, 31, v6
	v_lshlrev_b64 v[6:7], 10, v[6:7]
	v_lshl_add_u64 v[12:13], v[10:11], 0, v[6:7]
	ds_read_b128 v[6:9], v146 offset:3456
	s_waitcnt lgkmcnt(1)
	global_store_dwordx4 v[12:13], v[2:5], off nt
	v_mov_b64_e32 v[50:51], v[62:63]
	v_mov_b64_e32 v[72:73], v[68:69]
	v_or_b32_e32 v2, s11, v145
	v_ashrrev_i32_e32 v3, 31, v2
	v_lshlrev_b64 v[2:3], 10, v[2:3]
	v_lshl_add_u64 v[2:3], v[10:11], 0, v[2:3]
	s_waitcnt lgkmcnt(0)
	global_store_dwordx4 v[2:3], v[6:9], off nt
	s_waitcnt lgkmcnt(0)
	v_mov_b64_e32 v[2:3], v[102:103]
	v_mov_b64_e32 v[10:11], v[90:91]
	v_mov_b64_e32 v[6:7], v[106:107]
	v_mov_b64_e32 v[76:77], v[56:57]
	v_mov_b64_e32 v[88:89], v[60:61]
	v_mov_b64_e32 v[100:101], v[40:41]
	v_mov_b64_e32 v[112:113], v[44:45]
	v_mov_b64_e32 v[116:117], v[28:29]
	v_mov_b64_e32 v[120:121], v[32:33]
	v_mov_b64_e32 v[124:125], v[16:17]
	v_mov_b64_e32 v[128:129], v[20:21]
	s_andn2_b64 vcc, exec, s[6:7]
	v_mov_b64_e32 v[4:5], v[104:105]
	v_mov_b64_e32 v[8:9], v[108:109]
	v_mov_b64_e32 v[12:13], v[92:93]
	v_mov_b64_e32 v[24:25], v[96:97]
	v_mov_b64_e32 v[36:37], v[80:81]
	v_mov_b64_e32 v[48:49], v[84:85]
	v_mov_b64_e32 v[52:53], v[64:65]
	v_mov_b64_e32 v[70:71], v[66:67]
	v_mov_b64_e32 v[74:75], v[54:55]
	v_mov_b64_e32 v[86:87], v[58:59]
	v_mov_b64_e32 v[98:99], v[38:39]
	v_mov_b64_e32 v[110:111], v[42:43]
	v_mov_b64_e32 v[114:115], v[26:27]
	v_mov_b64_e32 v[118:119], v[30:31]
	v_mov_b64_e32 v[122:123], v[14:15]
	v_mov_b64_e32 v[126:127], v[18:19]
	s_mov_b32 s8, s10
	s_cbranch_vccz .LBB0_121
